# P16: leading half starts its epilogue during the trailing half's last MFMA block (align barrier moved after 2 row groups)
# baseline (speedup 1.0000x reference)
; #define PG8_STAGE(bufoff, gbase, o0, o1) do { \
;         __builtin_amdgcn_global_load_lds((const unsigned*)((const char*)(gbase) + (o0)), (LAS unsigned*)(lds + (bufoff) + ldsw), 16, 0, 0); \
;         __builtin_amdgcn_global_load_lds((const unsigned*)((const char*)(gbase) + (o1)), (LAS unsigned*)(lds + (bufoff) + ldsw + 8192), 16, 0, 0); } while (0)
; #define PG8_LDA(dst, b, h) do { _Pragma("unroll") for (int m = 0; m < 4; ++m) _Pragma("unroll") for (int k = 0; k < 2; ++k) dst[m][k] = *(const LAS bf16x8*)(lds + PG8_SA(b, h) + aoff + m * 2048 + k * 1024); } while (0)
; #define PG8_LDB(dst, b, h) do { _Pragma("unroll") for (int n = 0; n < 2; ++n) _Pragma("unroll") for (int k = 0; k < 2; ++k) dst[n][k] = *(const LAS bf16x8*)(lds + PG8_SB(b, h) + boff + n * 2048 + k * 1024); } while (0)
; #define PG8_WAIT_V(n) asm volatile("s_waitcnt vmcnt(" #n ")" ::: "memory")
; #define PG8_WAIT_L(n) asm volatile("s_waitcnt lgkmcnt(" #n ")" ::: "memory")
; #define PG8_BAR __builtin_amdgcn_s_barrier()
; #define PG8_SCHED __builtin_amdgcn_sched_barrier(0)
; template <class Epi, class Sched, class Prob>
; __device__ __forceinline__ void gemm_phase(LAS unsigned char* lds, LAS unsigned char* lds_epi, const Prob g, const Sched& S, const Epi& E, int wid) {
;     ...
;             PG8_LDB(B0, 0, 0); PG8_LDB(B1, 0, 1); PG8_SCHED; PG8_LDA(At, 0, 0); PG8_STAGE(PG8_SA(1, 1), a1, cA10, cA11);
;             PG8_WAIT_V(8); PG8_WAIT_L(0); PG8_BAR; PG8_MMA(0, 0, At, B0); PG8_MMA(0, 1, At, B1); PG8_BAR; PG8_SCHED;
;             PG8_LDA(At, 0, 1); PG8_STAGE(PG8_SB(0, 0), b2, vB0, vB1); PG8_STAGE(PG8_SB(0, 1), b2 + hstepB, vB0, vB1); PG8_STAGE(PG8_SA(0, 0), a2, cA00, cA01);
;             PG8_WAIT_V(8); PG8_WAIT_L(0); PG8_BAR; PG8_MMA(1, 0, At, B0); PG8_MMA(1, 1, At, B1); PG8_BAR; PG8_SCHED;
.LBB0_2091:
	ds_read_b128 v[24:27], v199
	ds_read_b128 v[28:31], v199 offset:1024
	ds_read_b128 v[16:19], v199 offset:2048
	ds_read_b128 v[20:23], v199 offset:3072
	ds_read_b128 v[8:11], v200
	ds_read_b128 v[12:15], v200 offset:1024
	ds_read_b128 v[0:3], v200 offset:2048
	ds_read_b128 v[4:7], v200 offset:3072
	s_add_u32 s40, s36, 0x80
	s_addc_u32 s41, s37, 0
	s_cmp_eq_u32 s69, 12
	s_cselect_b64 vcc, -1, 0
	s_cselect_b32 s41, s11, s41
	s_cselect_b32 s40, s29, s40
	v_cndmask_b32_e32 v185, v183, v181, vcc
	v_cndmask_b32_e32 v184, v182, v180, vcc
	v_lshl_add_u64 v[228:229], s[36:37], 0, v[176:177]
	s_add_i32 m0, s35, 0xc000
	ds_read_b128 v[186:189], v201
	ds_read_b128 v[190:193], v201 offset:1024
	ds_read_b128 v[204:207], v201 offset:2048
	ds_read_b128 v[208:211], v201 offset:3072
	ds_read_b128 v[212:215], v201 offset:4096
	ds_read_b128 v[216:219], v201 offset:5120
	ds_read_b128 v[220:223], v201 offset:6144
	ds_read_b128 v[224:227], v201 offset:7168
	global_load_lds_dwordx4 v[228:229], off
	v_lshl_add_u64 v[228:229], s[36:37], 0, v[174:175]
	s_add_i32 m0, s35, 0xe000
	s_nop 0
	global_load_lds_dwordx4 v[228:229], off
	s_waitcnt vmcnt(8)
	s_waitcnt lgkmcnt(0)
	s_barrier
	s_setprio 1
	s_waitcnt lgkmcnt(0)
	v_mfma_f32_16x16x128_f8f6f4 v[156:159], v[24:31], v[186:193], v[156:159]
	v_mfma_f32_16x16x128_f8f6f4 v[152:155], v[16:23], v[186:193], v[152:155]
	v_mfma_f32_16x16x128_f8f6f4 v[140:143], v[24:31], v[204:211], v[140:143]
	v_mfma_f32_16x16x128_f8f6f4 v[136:139], v[16:23], v[204:211], v[136:139]
	v_mfma_f32_16x16x128_f8f6f4 v[124:127], v[24:31], v[212:219], v[124:127]
	v_mfma_f32_16x16x128_f8f6f4 v[120:123], v[16:23], v[212:219], v[120:123]
	v_mfma_f32_16x16x128_f8f6f4 v[108:111], v[24:31], v[220:227], v[108:111]
	v_mfma_f32_16x16x128_f8f6f4 v[104:107], v[16:23], v[220:227], v[104:107]
	s_setprio 0
	s_setprio 1
	v_mfma_f32_16x16x128_f8f6f4 v[148:151], v[8:15], v[186:193], v[148:151]
	v_mfma_f32_16x16x128_f8f6f4 v[144:147], v[0:7], v[186:193], v[144:147]
	v_mfma_f32_16x16x128_f8f6f4 v[132:135], v[8:15], v[204:211], v[132:135]
	v_mfma_f32_16x16x128_f8f6f4 v[128:131], v[0:7], v[204:211], v[128:131]
	v_mfma_f32_16x16x128_f8f6f4 v[116:119], v[8:15], v[212:219], v[116:119]
	v_mfma_f32_16x16x128_f8f6f4 v[112:115], v[0:7], v[212:219], v[112:115]
	v_mfma_f32_16x16x128_f8f6f4 v[100:103], v[8:15], v[220:227], v[100:103]
	v_mfma_f32_16x16x128_f8f6f4 v[96:99], v[0:7], v[220:227], v[96:99]
	s_setprio 0
	s_barrier
	s_add_i32 s70, s63, s97
	v_lshl_add_u64 v[186:187], v[184:185], 0, v[160:161]
	s_mov_b32 m0, s70
	ds_read_b128 v[204:207], v201 offset:16384
	ds_read_b128 v[208:211], v201 offset:17408
	ds_read_b128 v[212:215], v201 offset:18432
	ds_read_b128 v[216:219], v201 offset:19456
	ds_read_b128 v[220:223], v201 offset:20480
	ds_read_b128 v[224:227], v201 offset:21504
	ds_read_b128 v[228:231], v201 offset:22528
	ds_read_b128 v[232:235], v201 offset:23552
	global_load_lds_dwordx4 v[186:187], off
	v_lshl_add_u64 v[188:189], v[184:185], 0, v[162:163]
	s_add_i32 m0, s70, 0x2000
	v_lshl_add_u64 v[190:191], v[184:185], 0, s[12:13]
	s_add_i32 s70, s64, s97
	global_load_lds_dwordx4 v[188:189], off
	v_lshl_add_u64 v[192:193], v[190:191], 0, v[160:161]
	s_mov_b32 m0, s70
	v_lshl_add_u64 v[190:191], v[190:191], 0, v[162:163]
	global_load_lds_dwordx4 v[192:193], off
	s_add_i32 m0, s70, 0x2000
	v_lshl_add_u64 v[192:193], s[40:41], 0, v[168:169]
	global_load_lds_dwordx4 v[190:191], off
	v_lshl_add_u64 v[190:191], s[40:41], 0, v[164:165]
	s_mov_b32 m0, s35
	s_nop 0
	global_load_lds_dwordx4 v[190:191], off
	s_mov_b32 m0, s58
	s_nop 0
	global_load_lds_dwordx4 v[192:193], off
	s_waitcnt vmcnt(8)
	s_waitcnt lgkmcnt(0)
	s_barrier
	s_setprio 1
	s_waitcnt lgkmcnt(0)
	v_mfma_f32_16x16x128_f8f6f4 v[92:95], v[24:31], v[204:211], v[92:95]
	v_mfma_f32_16x16x128_f8f6f4 v[88:91], v[16:23], v[204:211], v[88:91]
	v_mfma_f32_16x16x128_f8f6f4 v[76:79], v[24:31], v[212:219], v[76:79]
	v_mfma_f32_16x16x128_f8f6f4 v[72:75], v[16:23], v[212:219], v[72:75]
	v_mfma_f32_16x16x128_f8f6f4 v[60:63], v[24:31], v[220:227], v[60:63]
	v_mfma_f32_16x16x128_f8f6f4 v[56:59], v[16:23], v[220:227], v[56:59]
	v_mfma_f32_16x16x128_f8f6f4 v[44:47], v[24:31], v[228:235], v[44:47]
	v_mfma_f32_16x16x128_f8f6f4 v[40:43], v[16:23], v[228:235], v[40:43]
	s_setprio 0
	s_setprio 1
	v_mfma_f32_16x16x128_f8f6f4 v[84:87], v[8:15], v[204:211], v[84:87]
	v_mfma_f32_16x16x128_f8f6f4 v[80:83], v[0:7], v[204:211], v[80:83]
	v_mfma_f32_16x16x128_f8f6f4 v[68:71], v[8:15], v[212:219], v[68:71]
	v_mfma_f32_16x16x128_f8f6f4 v[64:67], v[0:7], v[212:219], v[64:67]
	v_mfma_f32_16x16x128_f8f6f4 v[52:55], v[8:15], v[220:227], v[52:55]
	v_mfma_f32_16x16x128_f8f6f4 v[48:51], v[0:7], v[220:227], v[48:51]
	v_mfma_f32_16x16x128_f8f6f4 v[36:39], v[8:15], v[228:235], v[36:39]
	v_mfma_f32_16x16x128_f8f6f4 v[32:35], v[0:7], v[228:235], v[32:35]
	s_setprio 0
	s_barrier
; #define LAS __attribute__((address_space(3)))
; #define PG8_STAGE(bufoff, gbase, o0, o1) do { \
;         __builtin_amdgcn_global_load_lds((const unsigned*)((const char*)(gbase) + (o0)), (LAS unsigned*)(lds + (bufoff) + ldsw), 16, 0, 0); \
;         __builtin_amdgcn_global_load_lds((const unsigned*)((const char*)(gbase) + (o1)), (LAS unsigned*)(lds + (bufoff) + ldsw + 8192), 16, 0, 0); } while (0)
; #define PG8_LDA(dst, b, h) do { _Pragma("unroll") for (int m = 0; m < 4; ++m) _Pragma("unroll") for (int k = 0; k < 2; ++k) dst[m][k] = *(const LAS bf16x8*)(lds + PG8_SA(b, h) + aoff + m * 2048 + k * 1024); } while (0)
; #define PG8_LDB(dst, b, h) do { _Pragma("unroll") for (int n = 0; n < 2; ++n) _Pragma("unroll") for (int k = 0; k < 2; ++k) dst[n][k] = *(const LAS bf16x8*)(lds + PG8_SB(b, h) + boff + n * 2048 + k * 1024); } while (0)
; #define PG8_WAIT_V(n) asm volatile("s_waitcnt vmcnt(" #n ")" ::: "memory")
; #define PG8_WAIT_L(n) asm volatile("s_waitcnt lgkmcnt(" #n ")" ::: "memory")
; #define PG8_BAR __builtin_amdgcn_s_barrier()
; #define PG8_SCHED __builtin_amdgcn_sched_barrier(0)
; template <class Epi, class Sched, class Prob>
; __device__ __forceinline__ void gemm_phase(LAS unsigned char* lds, LAS unsigned char* lds_epi, const Prob g, const Sched& S, const Epi& E, int wid) {
;     ...
;             PG8_LDB(B0, 1, 0); PG8_LDB(B1, 1, 1); PG8_SCHED; PG8_LDA(At, 1, 0); PG8_STAGE(PG8_SA(0, 1), a2, cA10, cA11);
;             PG8_WAIT_V(8); PG8_WAIT_L(0); PG8_BAR; PG8_MMA(0, 0, At, B0); PG8_MMA(0, 1, At, B1); PG8_BAR; PG8_SCHED;
;             PG8_LDA(At, 1, 1); PG8_STAGE(PG8_SB(1, 0), b3, vB0, vB1); PG8_STAGE(PG8_SB(1, 1), b3 + hstepB, vB0, vB1); PG8_STAGE(PG8_SA(1, 0), a3, cA00, cA01);
;             PG8_WAIT_V(8); PG8_WAIT_L(0); PG8_BAR; PG8_MMA(1, 0, At, B0); PG8_MMA(1, 1, At, B1); PG8_BAR; PG8_SCHED;
;         }
;         if constexpr (Prob::FP8) asm volatile("s_nop 7\n\ts_nop 7\n\ts_nop 7" ::: "memory");
;         if (wr == 0) PG8_BAR;
;     __device__ __forceinline__ void operator()(Acc& acc, const Unit& u, int wr, int wc, int fr, int fq, LAS unsigned char* le, int wid, int lane, int& cpm) const {
;         LAS float* S = (LAS float*)le; const int tid = wid * 64 + lane, row0 = u.pm * 256;
;         if (cpm != u.pm) { cpm = u.pm; if (tid < 256) S[tid] = slot_rstd[row0 + tid] * (1.0f / W_UP_SCALE); EPI_BAR(); }
	s_add_i32 s70, 0, 0x18000
	s_add_i32 s71, 0, 0x1c000
	v_add_u32_e32 v12, s70, v195
	v_add_u32_e32 v28, s71, v195
	ds_read_b128 v[0:3], v12
	ds_read_b128 v[4:7], v12 offset:1024
	ds_read_b128 v[8:11], v12 offset:2048
	ds_read_b128 v[12:15], v12 offset:3072
	ds_read_b128 v[16:19], v28
	ds_read_b128 v[20:23], v28 offset:1024
	ds_read_b128 v[24:27], v28 offset:2048
	ds_read_b128 v[28:31], v28 offset:3072
	s_mov_b32 m0, s59
	v_lshl_add_u64 v[236:237], s[40:41], 0, v[166:167]
	ds_read_b128 v[204:207], v201 offset:32768
	ds_read_b128 v[208:211], v201 offset:33792
	ds_read_b128 v[212:215], v201 offset:34816
	ds_read_b128 v[216:219], v201 offset:35840
	ds_read_b128 v[220:223], v201 offset:36864
	ds_read_b128 v[224:227], v201 offset:37888
	ds_read_b128 v[228:231], v201 offset:38912
	ds_read_b128 v[232:235], v201 offset:39936
	global_load_lds_dwordx4 v[236:237], off
	v_lshl_add_u64 v[236:237], s[40:41], 0, v[170:171]
	s_mov_b32 m0, s60
	s_nop 0
	global_load_lds_dwordx4 v[236:237], off
	s_waitcnt vmcnt(8)
	s_waitcnt lgkmcnt(0)
	s_barrier
	s_setprio 1
	s_waitcnt lgkmcnt(0)
	v_mfma_f32_16x16x128_f8f6f4 v[156:159], v[0:7], v[204:211], v[156:159]
	v_mfma_f32_16x16x128_f8f6f4 v[152:155], v[8:15], v[204:211], v[152:155]
	v_mfma_f32_16x16x128_f8f6f4 v[140:143], v[0:7], v[212:219], v[140:143]
	v_mfma_f32_16x16x128_f8f6f4 v[136:139], v[8:15], v[212:219], v[136:139]
	v_mfma_f32_16x16x128_f8f6f4 v[124:127], v[0:7], v[220:227], v[124:127]
	v_mfma_f32_16x16x128_f8f6f4 v[120:123], v[8:15], v[220:227], v[120:123]
	v_mfma_f32_16x16x128_f8f6f4 v[108:111], v[0:7], v[228:235], v[108:111]
	v_mfma_f32_16x16x128_f8f6f4 v[104:107], v[8:15], v[228:235], v[104:107]
	s_setprio 0
	s_setprio 1
	v_mfma_f32_16x16x128_f8f6f4 v[148:151], v[16:23], v[204:211], v[148:151]
	v_mfma_f32_16x16x128_f8f6f4 v[144:147], v[24:31], v[204:211], v[144:147]
	v_mfma_f32_16x16x128_f8f6f4 v[132:135], v[16:23], v[212:219], v[132:135]
	v_mfma_f32_16x16x128_f8f6f4 v[128:131], v[24:31], v[212:219], v[128:131]
	v_mfma_f32_16x16x128_f8f6f4 v[116:119], v[16:23], v[220:227], v[116:119]
	v_mfma_f32_16x16x128_f8f6f4 v[112:115], v[24:31], v[220:227], v[112:115]
	v_mfma_f32_16x16x128_f8f6f4 v[100:103], v[16:23], v[228:235], v[100:103]
	v_mfma_f32_16x16x128_f8f6f4 v[96:99], v[24:31], v[228:235], v[96:99]
	s_setprio 0
	s_barrier
	s_add_i32 s40, s70, s97
	v_lshl_add_u64 v[186:187], v[186:187], 0, s[18:19]
	s_mov_b32 m0, s40
	ds_read_b128 v[204:207], v201 offset:49152
	ds_read_b128 v[208:211], v201 offset:50176
	ds_read_b128 v[212:215], v201 offset:51200
	ds_read_b128 v[216:219], v201 offset:52224
	ds_read_b128 v[220:223], v201 offset:53248
	ds_read_b128 v[224:227], v201 offset:54272
	ds_read_b128 v[228:231], v201 offset:55296
	ds_read_b128 v[232:235], v201 offset:56320
	global_load_lds_dwordx4 v[186:187], off
	v_lshl_add_u64 v[186:187], v[188:189], 0, s[18:19]
	s_add_i32 m0, s40, 0x2000
	v_lshl_add_u64 v[184:185], v[184:185], 0, s[20:21]
	s_add_i32 s40, s71, s97
	global_load_lds_dwordx4 v[186:187], off
	v_lshl_add_u64 v[186:187], v[184:185], 0, v[160:161]
	s_mov_b32 m0, s40
	v_lshl_add_u64 v[184:185], v[184:185], 0, v[162:163]
	global_load_lds_dwordx4 v[186:187], off
	s_add_i32 m0, s40, 0x2000
	s_nop 0
	global_load_lds_dwordx4 v[184:185], off
	v_lshl_add_u64 v[184:185], v[190:191], 0, s[18:19]
	s_mov_b32 m0, s61
	s_nop 0
	global_load_lds_dwordx4 v[184:185], off
	v_lshl_add_u64 v[184:185], v[192:193], 0, s[18:19]
	s_mov_b32 m0, s62
	s_nop 0
	global_load_lds_dwordx4 v[184:185], off
	s_waitcnt vmcnt(8)
	s_waitcnt lgkmcnt(0)
	s_barrier
	s_setprio 1
	s_waitcnt lgkmcnt(0)
	v_mfma_f32_16x16x128_f8f6f4 v[92:95], v[0:7], v[204:211], v[92:95]
	v_mfma_f32_16x16x128_f8f6f4 v[88:91], v[8:15], v[204:211], v[88:91]
	v_mfma_f32_16x16x128_f8f6f4 v[76:79], v[0:7], v[212:219], v[76:79]
	v_mfma_f32_16x16x128_f8f6f4 v[72:75], v[8:15], v[212:219], v[72:75]
	v_mfma_f32_16x16x128_f8f6f4 v[60:63], v[0:7], v[220:227], v[60:63]
	v_mfma_f32_16x16x128_f8f6f4 v[56:59], v[8:15], v[220:227], v[56:59]
	v_mfma_f32_16x16x128_f8f6f4 v[44:47], v[0:7], v[228:235], v[44:47]
	v_mfma_f32_16x16x128_f8f6f4 v[40:43], v[8:15], v[228:235], v[40:43]
	s_setprio 0
	s_setprio 1
	v_mfma_f32_16x16x128_f8f6f4 v[84:87], v[16:23], v[204:211], v[84:87]
	v_mfma_f32_16x16x128_f8f6f4 v[80:83], v[24:31], v[204:211], v[80:83]
	v_mfma_f32_16x16x128_f8f6f4 v[68:71], v[16:23], v[212:219], v[68:71]
	v_mfma_f32_16x16x128_f8f6f4 v[64:67], v[24:31], v[212:219], v[64:67]
	v_mfma_f32_16x16x128_f8f6f4 v[52:55], v[16:23], v[220:227], v[52:55]
	v_mfma_f32_16x16x128_f8f6f4 v[48:51], v[24:31], v[220:227], v[48:51]
	v_mfma_f32_16x16x128_f8f6f4 v[36:39], v[16:23], v[228:235], v[36:39]
	v_mfma_f32_16x16x128_f8f6f4 v[32:35], v[24:31], v[228:235], v[32:35]
	s_setprio 0
	s_barrier
	s_add_i32 s69, s69, 2
	s_add_u32 s36, s36, 0x100
	s_addc_u32 s37, s37, 0
	s_cmp_gt_u32 s69, 13
	v_lshl_add_u64 v[182:183], v[182:183], 0, s[22:23]
	s_cbranch_scc0 .LBB0_2091
	s_nop 7
	s_nop 7
	s_nop 7
.LBB0_2094:
	s_lshl_b32 s11, s67, 8
	s_cmp_eq_u32 s68, s67
	s_cbranch_scc1 .LBB0_2098
	s_and_saveexec_b64 s[36:37], s[6:7]
	s_cbranch_execz .LBB0_2097
	v_add_u32_e32 v0, s11, v196
	v_ashrrev_i32_e32 v1, 31, v0
	v_lshl_add_u64 v[0:1], v[0:1], 2, s[16:17]
	global_load_dword v0, v[0:1], off
	s_waitcnt vmcnt(0)
	v_mul_f32_e32 v0, 0x3b800000, v0
	ds_write_b32 v197, v0

; #define NEXT_ROW(roff, m, LD) do { roff += (size_t)((m) == 3 ? 80 : 16) * (LD); asm volatile("" : "+v"(roff) :: "memory"); } while (0)
;     __device__ __forceinline__ void operator()(Acc& acc, const Unit& u, int wr, int wc, int fr, int fq, LAS unsigned char* le, int wid, int lane, int& cpm) const {
;     ...
;         size_t roff = (size_t)(row0 + wr * 64 + fr) * DFF + u.pn * 128 + wc * 32 + fq * 8;
; #pragma unroll
;         for (int ai = 0; ai < 2; ++ai)
; #pragma unroll
;             for (int m = 0; m < 4; ++m) { const int rt = ai * 128 + wr * 64 + m * 16 + fr; const float rs = S[rt];
;                 const float rl = rs * -1.4426950408889634f, kk = rs * rs * H_SCALE; f32x4 ha, hb;
; #pragma unroll
;                 for (int j = 0; j < 4; ++j) { const float g0 = acc[ai][0][m][0][j], g1 = acc[ai][0][m][1][j];
;                     ha[j] = (g0 * acc[ai][1][m][0][j]) * kk * __builtin_amdgcn_rcpf(1.0f + __builtin_amdgcn_exp2f(g0 * rl));
;                     hb[j] = (g1 * acc[ai][1][m][1][j]) * kk * __builtin_amdgcn_rcpf(1.0f + __builtin_amdgcn_exp2f(g1 * rl)); }
;                 u32x2 w; w.x = pk4_fp8(ha[0], ha[1], ha[2], ha[3]); w.y = pk4_fp8(hb[0], hb[1], hb[2], hb[3]);
;                 ST_NT((u32x2*)(out + roff), w);
;                 NEXT_ROW(roff, m, DFF); }
.LBB0_2098:
	ds_read_b32 v204, v198
	ds_read_b32 v205, v198 offset:64
	ds_read_b32 v206, v198 offset:128
	ds_read_b32 v207, v198 offset:192
	ds_read_b32 v208, v198 offset:512
	ds_read_b32 v209, v198 offset:576
	ds_read_b32 v210, v198 offset:640
	ds_read_b32 v211, v198 offset:704
	s_lshl_b32 s36, s34, 7
	s_ashr_i32 s37, s36, 31
	v_add_u32_e32 v4, s11, v194
	v_lshl_add_u64 v[0:1], v[172:173], 0, s[36:37]
	v_mad_i64_i32 v[0:1], s[36:37], v4, s65, v[0:1]
	v_lshl_add_u64 v[0:1], s[14:15], 0, v[0:1]
	s_waitcnt lgkmcnt(0)
	v_mul_f32_e32 v212, 0xbfb8aa3b, v204
	v_mul_f32_e32 v214, v204, v204
	v_pk_mul_f32 v[224:225], v[156:157], v[148:149]
	v_pk_mul_f32 v[226:227], v[158:159], v[150:151]
	v_pk_mul_f32 v[228:229], v[152:153], v[144:145]
	v_pk_mul_f32 v[230:231], v[154:155], v[146:147]
	v_mul_f32_e32 v214, 0x41000000, v214
	v_pk_mul_f32 v[216:217], v[156:157], v[212:213] op_sel_hi:[1,0]
	v_pk_mul_f32 v[218:219], v[158:159], v[212:213] op_sel_hi:[1,0]
	v_pk_mul_f32 v[220:221], v[152:153], v[212:213] op_sel_hi:[1,0]
	v_pk_mul_f32 v[222:223], v[154:155], v[212:213] op_sel_hi:[1,0]
	v_rcp_f32_e32 v214, v214
	v_exp_f32_e32 v216, v216
	v_exp_f32_e32 v217, v217
	v_exp_f32_e32 v218, v218
	v_exp_f32_e32 v219, v219
	v_exp_f32_e32 v220, v220
	v_exp_f32_e32 v221, v221
	v_exp_f32_e32 v222, v222
	v_exp_f32_e32 v223, v223
	v_pk_fma_f32 v[216:217], v[216:217], v[214:215], v[214:215] op_sel_hi:[1,0,0]
	v_pk_fma_f32 v[218:219], v[218:219], v[214:215], v[214:215] op_sel_hi:[1,0,0]
	v_pk_fma_f32 v[220:221], v[220:221], v[214:215], v[214:215] op_sel_hi:[1,0,0]
	v_pk_fma_f32 v[222:223], v[222:223], v[214:215], v[214:215] op_sel_hi:[1,0,0]
	v_rcp_f32_e32 v216, v216
	v_rcp_f32_e32 v217, v217
	v_rcp_f32_e32 v218, v218
	v_rcp_f32_e32 v219, v219
	v_rcp_f32_e32 v220, v220
	v_rcp_f32_e32 v221, v221
	v_rcp_f32_e32 v222, v222
	v_rcp_f32_e32 v223, v223
	v_pk_mul_f32 v[224:225], v[224:225], v[216:217]
	v_pk_mul_f32 v[226:227], v[226:227], v[218:219]
	v_pk_mul_f32 v[228:229], v[228:229], v[220:221]
	v_pk_mul_f32 v[230:231], v[230:231], v[222:223]
	v_med3_f32 v224, v224, s66, v202
	v_med3_f32 v225, v225, s66, v202
	v_med3_f32 v226, v226, s66, v202
	v_med3_f32 v227, v227, s66, v202
	v_med3_f32 v228, v228, s66, v202
	v_med3_f32 v229, v229, s66, v202
	v_med3_f32 v230, v230, s66, v202
	v_med3_f32 v231, v231, s66, v202
	v_cvt_pk_fp8_f32 v2, v224, v225
	v_cvt_pk_fp8_f32 v3, v228, v229
	v_cvt_pk_fp8_f32 v2, v226, v227 op_sel:[0,0,1]
	v_cvt_pk_fp8_f32 v3, v230, v231 op_sel:[0,0,1]
	s_nop 0
	global_store_dwordx2 v[0:1], v[2:3], off
	v_lshl_add_u64 v[0:1], v[0:1], 0, s[24:25]
	v_mul_f32_e32 v212, 0xbfb8aa3b, v205
	v_mul_f32_e32 v214, v205, v205
	v_pk_mul_f32 v[224:225], v[140:141], v[132:133]
	v_pk_mul_f32 v[226:227], v[142:143], v[134:135]
	v_pk_mul_f32 v[228:229], v[136:137], v[128:129]
	v_pk_mul_f32 v[230:231], v[138:139], v[130:131]
	v_mul_f32_e32 v214, 0x41000000, v214
	v_pk_mul_f32 v[216:217], v[140:141], v[212:213] op_sel_hi:[1,0]
	v_pk_mul_f32 v[218:219], v[142:143], v[212:213] op_sel_hi:[1,0]
	v_pk_mul_f32 v[220:221], v[136:137], v[212:213] op_sel_hi:[1,0]
	v_pk_mul_f32 v[222:223], v[138:139], v[212:213] op_sel_hi:[1,0]
	v_rcp_f32_e32 v214, v214
	v_exp_f32_e32 v216, v216
	v_exp_f32_e32 v217, v217
	v_exp_f32_e32 v218, v218
	v_exp_f32_e32 v219, v219
	v_exp_f32_e32 v220, v220
	v_exp_f32_e32 v221, v221
	v_exp_f32_e32 v222, v222
	v_exp_f32_e32 v223, v223
	v_pk_fma_f32 v[216:217], v[216:217], v[214:215], v[214:215] op_sel_hi:[1,0,0]
	v_pk_fma_f32 v[218:219], v[218:219], v[214:215], v[214:215] op_sel_hi:[1,0,0]
	v_pk_fma_f32 v[220:221], v[220:221], v[214:215], v[214:215] op_sel_hi:[1,0,0]
	v_pk_fma_f32 v[222:223], v[222:223], v[214:215], v[214:215] op_sel_hi:[1,0,0]
	v_rcp_f32_e32 v216, v216
	v_rcp_f32_e32 v217, v217
	v_rcp_f32_e32 v218, v218
	v_rcp_f32_e32 v219, v219
	v_rcp_f32_e32 v220, v220
	v_rcp_f32_e32 v221, v221
	v_rcp_f32_e32 v222, v222
	v_rcp_f32_e32 v223, v223
	v_pk_mul_f32 v[224:225], v[224:225], v[216:217]
	v_pk_mul_f32 v[226:227], v[226:227], v[218:219]
	v_pk_mul_f32 v[228:229], v[228:229], v[220:221]
	v_pk_mul_f32 v[230:231], v[230:231], v[222:223]
	v_med3_f32 v224, v224, s66, v202
	v_med3_f32 v225, v225, s66, v202
	v_med3_f32 v226, v226, s66, v202
	v_med3_f32 v227, v227, s66, v202
	v_med3_f32 v228, v228, s66, v202
	v_med3_f32 v229, v229, s66, v202
	v_med3_f32 v230, v230, s66, v202
	v_med3_f32 v231, v231, s66, v202
	v_cvt_pk_fp8_f32 v2, v224, v225
	v_cvt_pk_fp8_f32 v3, v228, v229
	v_cvt_pk_fp8_f32 v2, v226, v227 op_sel:[0,0,1]
	v_cvt_pk_fp8_f32 v3, v230, v231 op_sel:[0,0,1]
	s_nop 0
	global_store_dwordx2 v[0:1], v[2:3], off
	v_lshl_add_u64 v[0:1], v[0:1], 0, s[24:25]
	v_readlane_b32 s36, v254, 27
	v_readlane_b32 s37, v254, 28
	s_and_b64 vcc, exec, s[36:37]
	s_cbranch_vccz .Lp16_align_skip
	s_barrier
; #define NEXT_ROW(roff, m, LD) do { roff += (size_t)((m) == 3 ? 80 : 16) * (LD); asm volatile("" : "+v"(roff) :: "memory"); } while (0)
;     __device__ __forceinline__ void operator()(Acc& acc, const Unit& u, int wr, int wc, int fr, int fq, LAS unsigned char* le, int wid, int lane, int& cpm) const {
;     ...
;             for (int m = 0; m < 4; ++m) { const int rt = ai * 128 + wr * 64 + m * 16 + fr; const float rs = S[rt];
;                 const float rl = rs * -1.4426950408889634f, kk = rs * rs * H_SCALE; f32x4 ha, hb;
; #pragma unroll
;                 for (int j = 0; j < 4; ++j) { const float g0 = acc[ai][0][m][0][j], g1 = acc[ai][0][m][1][j];
;                     ha[j] = (g0 * acc[ai][1][m][0][j]) * kk * __builtin_amdgcn_rcpf(1.0f + __builtin_amdgcn_exp2f(g0 * rl));
;                     hb[j] = (g1 * acc[ai][1][m][1][j]) * kk * __builtin_amdgcn_rcpf(1.0f + __builtin_amdgcn_exp2f(g1 * rl)); }
;                 u32x2 w; w.x = pk4_fp8(ha[0], ha[1], ha[2], ha[3]); w.y = pk4_fp8(hb[0], hb[1], hb[2], hb[3]);
;                 ST_NT((u32x2*)(out + roff), w);
;                 NEXT_ROW(roff, m, DFF); }
.Lp16_align_skip:
	v_mul_f32_e32 v212, 0xbfb8aa3b, v206
	v_mul_f32_e32 v214, v206, v206
	v_pk_mul_f32 v[224:225], v[124:125], v[116:117]
	v_pk_mul_f32 v[226:227], v[126:127], v[118:119]
	v_pk_mul_f32 v[228:229], v[120:121], v[112:113]
	v_pk_mul_f32 v[230:231], v[122:123], v[114:115]
	v_mul_f32_e32 v214, 0x41000000, v214
	v_pk_mul_f32 v[216:217], v[124:125], v[212:213] op_sel_hi:[1,0]
	v_pk_mul_f32 v[218:219], v[126:127], v[212:213] op_sel_hi:[1,0]
	v_pk_mul_f32 v[220:221], v[120:121], v[212:213] op_sel_hi:[1,0]
	v_pk_mul_f32 v[222:223], v[122:123], v[212:213] op_sel_hi:[1,0]
	v_rcp_f32_e32 v214, v214
	v_exp_f32_e32 v216, v216
	v_exp_f32_e32 v217, v217
	v_exp_f32_e32 v218, v218
	v_exp_f32_e32 v219, v219
	v_exp_f32_e32 v220, v220
	v_exp_f32_e32 v221, v221
	v_exp_f32_e32 v222, v222
	v_exp_f32_e32 v223, v223
	v_pk_fma_f32 v[216:217], v[216:217], v[214:215], v[214:215] op_sel_hi:[1,0,0]
	v_pk_fma_f32 v[218:219], v[218:219], v[214:215], v[214:215] op_sel_hi:[1,0,0]
	v_pk_fma_f32 v[220:221], v[220:221], v[214:215], v[214:215] op_sel_hi:[1,0,0]
	v_pk_fma_f32 v[222:223], v[222:223], v[214:215], v[214:215] op_sel_hi:[1,0,0]
	v_rcp_f32_e32 v216, v216
	v_rcp_f32_e32 v217, v217
	v_rcp_f32_e32 v218, v218
	v_rcp_f32_e32 v219, v219
	v_rcp_f32_e32 v220, v220
	v_rcp_f32_e32 v221, v221
	v_rcp_f32_e32 v222, v222
	v_rcp_f32_e32 v223, v223
	v_pk_mul_f32 v[224:225], v[224:225], v[216:217]
	v_pk_mul_f32 v[226:227], v[226:227], v[218:219]
	v_pk_mul_f32 v[228:229], v[228:229], v[220:221]
	v_pk_mul_f32 v[230:231], v[230:231], v[222:223]
	v_med3_f32 v224, v224, s66, v202
	v_med3_f32 v225, v225, s66, v202
	v_med3_f32 v226, v226, s66, v202
	v_med3_f32 v227, v227, s66, v202
	v_med3_f32 v228, v228, s66, v202
	v_med3_f32 v229, v229, s66, v202
	v_med3_f32 v230, v230, s66, v202
	v_med3_f32 v231, v231, s66, v202
	v_cvt_pk_fp8_f32 v2, v224, v225
	v_cvt_pk_fp8_f32 v3, v228, v229
	v_cvt_pk_fp8_f32 v2, v226, v227 op_sel:[0,0,1]
	v_cvt_pk_fp8_f32 v3, v230, v231 op_sel:[0,0,1]
	s_nop 0
	global_store_dwordx2 v[0:1], v[2:3], off
	v_lshl_add_u64 v[0:1], v[0:1], 0, s[24:25]
	v_mul_f32_e32 v212, 0xbfb8aa3b, v207
	v_mul_f32_e32 v214, v207, v207
	v_pk_mul_f32 v[224:225], v[108:109], v[100:101]
	v_pk_mul_f32 v[226:227], v[110:111], v[102:103]
	v_pk_mul_f32 v[228:229], v[104:105], v[96:97]
	v_pk_mul_f32 v[230:231], v[106:107], v[98:99]
	v_mul_f32_e32 v214, 0x41000000, v214
	v_pk_mul_f32 v[216:217], v[108:109], v[212:213] op_sel_hi:[1,0]
	v_pk_mul_f32 v[218:219], v[110:111], v[212:213] op_sel_hi:[1,0]
	v_pk_mul_f32 v[220:221], v[104:105], v[212:213] op_sel_hi:[1,0]
	v_pk_mul_f32 v[222:223], v[106:107], v[212:213] op_sel_hi:[1,0]
	v_rcp_f32_e32 v214, v214
	v_exp_f32_e32 v216, v216
	v_exp_f32_e32 v217, v217
	v_exp_f32_e32 v218, v218
	v_exp_f32_e32 v219, v219
	v_exp_f32_e32 v220, v220
	v_exp_f32_e32 v221, v221
	v_exp_f32_e32 v222, v222
	v_exp_f32_e32 v223, v223
	v_pk_fma_f32 v[216:217], v[216:217], v[214:215], v[214:215] op_sel_hi:[1,0,0]
	v_pk_fma_f32 v[218:219], v[218:219], v[214:215], v[214:215] op_sel_hi:[1,0,0]
	v_pk_fma_f32 v[220:221], v[220:221], v[214:215], v[214:215] op_sel_hi:[1,0,0]
	v_pk_fma_f32 v[222:223], v[222:223], v[214:215], v[214:215] op_sel_hi:[1,0,0]
	v_rcp_f32_e32 v216, v216
	v_rcp_f32_e32 v217, v217
	v_rcp_f32_e32 v218, v218
	v_rcp_f32_e32 v219, v219
	v_rcp_f32_e32 v220, v220
	v_rcp_f32_e32 v221, v221
	v_rcp_f32_e32 v222, v222
	v_rcp_f32_e32 v223, v223
	v_pk_mul_f32 v[224:225], v[224:225], v[216:217]
	v_pk_mul_f32 v[226:227], v[226:227], v[218:219]
	v_pk_mul_f32 v[228:229], v[228:229], v[220:221]
	v_pk_mul_f32 v[230:231], v[230:231], v[222:223]
	v_med3_f32 v224, v224, s66, v202
	v_med3_f32 v225, v225, s66, v202
	v_med3_f32 v226, v226, s66, v202
	v_med3_f32 v227, v227, s66, v202
	v_med3_f32 v228, v228, s66, v202
	v_med3_f32 v229, v229, s66, v202
	v_med3_f32 v230, v230, s66, v202
	v_med3_f32 v231, v231, s66, v202
	v_cvt_pk_fp8_f32 v2, v224, v225
	v_cvt_pk_fp8_f32 v3, v228, v229
	v_cvt_pk_fp8_f32 v2, v226, v227 op_sel:[0,0,1]
	v_cvt_pk_fp8_f32 v3, v230, v231 op_sel:[0,0,1]
	s_nop 0
	global_store_dwordx2 v[0:1], v[2:3], off
	v_lshl_add_u64 v[0:1], v[0:1], 0, s[26:27]
	v_mul_f32_e32 v212, 0xbfb8aa3b, v208
	v_mul_f32_e32 v214, v208, v208
	v_pk_mul_f32 v[224:225], v[92:93], v[84:85]
	v_pk_mul_f32 v[226:227], v[94:95], v[86:87]
	v_pk_mul_f32 v[228:229], v[88:89], v[80:81]
	v_pk_mul_f32 v[230:231], v[90:91], v[82:83]
	v_mul_f32_e32 v214, 0x41000000, v214
	v_pk_mul_f32 v[216:217], v[92:93], v[212:213] op_sel_hi:[1,0]
	v_pk_mul_f32 v[218:219], v[94:95], v[212:213] op_sel_hi:[1,0]
	v_pk_mul_f32 v[220:221], v[88:89], v[212:213] op_sel_hi:[1,0]
	v_pk_mul_f32 v[222:223], v[90:91], v[212:213] op_sel_hi:[1,0]
	v_rcp_f32_e32 v214, v214
	v_exp_f32_e32 v216, v216
	v_exp_f32_e32 v217, v217
	v_exp_f32_e32 v218, v218
	v_exp_f32_e32 v219, v219
	v_exp_f32_e32 v220, v220
	v_exp_f32_e32 v221, v221
	v_exp_f32_e32 v222, v222
	v_exp_f32_e32 v223, v223
	v_pk_fma_f32 v[216:217], v[216:217], v[214:215], v[214:215] op_sel_hi:[1,0,0]
	v_pk_fma_f32 v[218:219], v[218:219], v[214:215], v[214:215] op_sel_hi:[1,0,0]
	v_pk_fma_f32 v[220:221], v[220:221], v[214:215], v[214:215] op_sel_hi:[1,0,0]
	v_pk_fma_f32 v[222:223], v[222:223], v[214:215], v[214:215] op_sel_hi:[1,0,0]
	v_rcp_f32_e32 v216, v216
	v_rcp_f32_e32 v217, v217
	v_rcp_f32_e32 v218, v218
	v_rcp_f32_e32 v219, v219
	v_rcp_f32_e32 v220, v220
	v_rcp_f32_e32 v221, v221
	v_rcp_f32_e32 v222, v222
	v_rcp_f32_e32 v223, v223
	v_pk_mul_f32 v[224:225], v[224:225], v[216:217]
	v_pk_mul_f32 v[226:227], v[226:227], v[218:219]
	v_pk_mul_f32 v[228:229], v[228:229], v[220:221]
	v_pk_mul_f32 v[230:231], v[230:231], v[222:223]
	v_med3_f32 v224, v224, s66, v202
; #define PG8_BAR __builtin_amdgcn_s_barrier()
; #define PG8_ACC_INIT(unit) do { if constexpr (Epi::ACC_INIT) { E.init(acc, unit, wr, wc, fr, fq); } else { \
;         _Pragma("unroll") for (int a = 0; a < 2; ++a) _Pragma("unroll") for (int b = 0; b < 2; ++b) _Pragma("unroll") for (int m = 0; m < 4; ++m) _Pragma("unroll") for (int n = 0; n < 2; ++n) acc[a][b][m][n] = (f32x4){0.f, 0.f, 0.f, 0.f}; } } while (0)
; #define NEXT_ROW(roff, m, LD) do { roff += (size_t)((m) == 3 ? 80 : 16) * (LD); asm volatile("" : "+v"(roff) :: "memory"); } while (0)
; template <class Epi, class Sched, class Prob>
; __device__ __forceinline__ void gemm_phase(LAS unsigned char* lds, LAS unsigned char* lds_epi, const Prob g, const Sched& S, const Epi& E, int wid) {
;     ...
;         if (!has_next) break;
;         PG8_ACC_INIT(nxt);
;         cur = nxt; cA = nA; cB = nB; ++ui;
;         if (wr == 1) PG8_BAR;
;     __device__ __forceinline__ void operator()(Acc& acc, const Unit& u, int wr, int wc, int fr, int fq, LAS unsigned char* le, int wid, int lane, int& cpm) const {
;     ...
;             for (int m = 0; m < 4; ++m) { const int rt = ai * 128 + wr * 64 + m * 16 + fr; const float rs = S[rt];
;                 const float rl = rs * -1.4426950408889634f, kk = rs * rs * H_SCALE; f32x4 ha, hb;
; #pragma unroll
;                 for (int j = 0; j < 4; ++j) { const float g0 = acc[ai][0][m][0][j], g1 = acc[ai][0][m][1][j];
;                     ha[j] = (g0 * acc[ai][1][m][0][j]) * kk * __builtin_amdgcn_rcpf(1.0f + __builtin_amdgcn_exp2f(g0 * rl));
;                     hb[j] = (g1 * acc[ai][1][m][1][j]) * kk * __builtin_amdgcn_rcpf(1.0f + __builtin_amdgcn_exp2f(g1 * rl)); }
;                 u32x2 w; w.x = pk4_fp8(ha[0], ha[1], ha[2], ha[3]); w.y = pk4_fp8(hb[0], hb[1], hb[2], hb[3]);
;                 ST_NT((u32x2*)(out + roff), w);
;                 NEXT_ROW(roff, m, DFF); }
	v_med3_f32 v225, v225, s66, v202
	v_med3_f32 v226, v226, s66, v202
	v_med3_f32 v227, v227, s66, v202
	v_med3_f32 v228, v228, s66, v202
	v_med3_f32 v229, v229, s66, v202
	v_med3_f32 v230, v230, s66, v202
	v_med3_f32 v231, v231, s66, v202
	v_cvt_pk_fp8_f32 v2, v224, v225
	v_cvt_pk_fp8_f32 v3, v228, v229
	v_cvt_pk_fp8_f32 v2, v226, v227 op_sel:[0,0,1]
	v_cvt_pk_fp8_f32 v3, v230, v231 op_sel:[0,0,1]
	s_nop 0
	global_store_dwordx2 v[0:1], v[2:3], off
	v_lshl_add_u64 v[0:1], v[0:1], 0, s[24:25]
	v_mul_f32_e32 v212, 0xbfb8aa3b, v209
	v_mul_f32_e32 v214, v209, v209
	v_pk_mul_f32 v[224:225], v[76:77], v[68:69]
	v_pk_mul_f32 v[226:227], v[78:79], v[70:71]
	v_pk_mul_f32 v[228:229], v[72:73], v[64:65]
	v_pk_mul_f32 v[230:231], v[74:75], v[66:67]
	v_mul_f32_e32 v214, 0x41000000, v214
	v_pk_mul_f32 v[216:217], v[76:77], v[212:213] op_sel_hi:[1,0]
	v_pk_mul_f32 v[218:219], v[78:79], v[212:213] op_sel_hi:[1,0]
	v_pk_mul_f32 v[220:221], v[72:73], v[212:213] op_sel_hi:[1,0]
	v_pk_mul_f32 v[222:223], v[74:75], v[212:213] op_sel_hi:[1,0]
	v_rcp_f32_e32 v214, v214
	v_exp_f32_e32 v216, v216
	v_exp_f32_e32 v217, v217
	v_exp_f32_e32 v218, v218
	v_exp_f32_e32 v219, v219
	v_exp_f32_e32 v220, v220
	v_exp_f32_e32 v221, v221
	v_exp_f32_e32 v222, v222
	v_exp_f32_e32 v223, v223
	v_pk_fma_f32 v[216:217], v[216:217], v[214:215], v[214:215] op_sel_hi:[1,0,0]
	v_pk_fma_f32 v[218:219], v[218:219], v[214:215], v[214:215] op_sel_hi:[1,0,0]
	v_pk_fma_f32 v[220:221], v[220:221], v[214:215], v[214:215] op_sel_hi:[1,0,0]
	v_pk_fma_f32 v[222:223], v[222:223], v[214:215], v[214:215] op_sel_hi:[1,0,0]
	v_rcp_f32_e32 v216, v216
	v_rcp_f32_e32 v217, v217
	v_rcp_f32_e32 v218, v218
	v_rcp_f32_e32 v219, v219
	v_rcp_f32_e32 v220, v220
	v_rcp_f32_e32 v221, v221
	v_rcp_f32_e32 v222, v222
	v_rcp_f32_e32 v223, v223
	v_pk_mul_f32 v[224:225], v[224:225], v[216:217]
	v_pk_mul_f32 v[226:227], v[226:227], v[218:219]
	v_pk_mul_f32 v[228:229], v[228:229], v[220:221]
	v_pk_mul_f32 v[230:231], v[230:231], v[222:223]
	v_med3_f32 v224, v224, s66, v202
	v_med3_f32 v225, v225, s66, v202
	v_med3_f32 v226, v226, s66, v202
	v_med3_f32 v227, v227, s66, v202
	v_med3_f32 v228, v228, s66, v202
	v_med3_f32 v229, v229, s66, v202
	v_med3_f32 v230, v230, s66, v202
	v_med3_f32 v231, v231, s66, v202
	v_cvt_pk_fp8_f32 v2, v224, v225
	v_cvt_pk_fp8_f32 v3, v228, v229
	v_cvt_pk_fp8_f32 v2, v226, v227 op_sel:[0,0,1]
	v_cvt_pk_fp8_f32 v3, v230, v231 op_sel:[0,0,1]
	s_nop 0
	global_store_dwordx2 v[0:1], v[2:3], off
	v_lshl_add_u64 v[0:1], v[0:1], 0, s[24:25]
	v_mul_f32_e32 v212, 0xbfb8aa3b, v210
	v_mul_f32_e32 v214, v210, v210
	v_pk_mul_f32 v[224:225], v[60:61], v[52:53]
	v_pk_mul_f32 v[226:227], v[62:63], v[54:55]
	v_pk_mul_f32 v[228:229], v[56:57], v[48:49]
	v_pk_mul_f32 v[230:231], v[58:59], v[50:51]
	v_mul_f32_e32 v214, 0x41000000, v214
	v_pk_mul_f32 v[216:217], v[60:61], v[212:213] op_sel_hi:[1,0]
	v_pk_mul_f32 v[218:219], v[62:63], v[212:213] op_sel_hi:[1,0]
	v_pk_mul_f32 v[220:221], v[56:57], v[212:213] op_sel_hi:[1,0]
	v_pk_mul_f32 v[222:223], v[58:59], v[212:213] op_sel_hi:[1,0]
	v_rcp_f32_e32 v214, v214
	v_exp_f32_e32 v216, v216
	v_exp_f32_e32 v217, v217
	v_exp_f32_e32 v218, v218
	v_exp_f32_e32 v219, v219
	v_exp_f32_e32 v220, v220
	v_exp_f32_e32 v221, v221
	v_exp_f32_e32 v222, v222
	v_exp_f32_e32 v223, v223
	v_pk_fma_f32 v[216:217], v[216:217], v[214:215], v[214:215] op_sel_hi:[1,0,0]
	v_pk_fma_f32 v[218:219], v[218:219], v[214:215], v[214:215] op_sel_hi:[1,0,0]
	v_pk_fma_f32 v[220:221], v[220:221], v[214:215], v[214:215] op_sel_hi:[1,0,0]
	v_pk_fma_f32 v[222:223], v[222:223], v[214:215], v[214:215] op_sel_hi:[1,0,0]
	v_rcp_f32_e32 v216, v216
	v_rcp_f32_e32 v217, v217
	v_rcp_f32_e32 v218, v218
	v_rcp_f32_e32 v219, v219
	v_rcp_f32_e32 v220, v220
	v_rcp_f32_e32 v221, v221
	v_rcp_f32_e32 v222, v222
	v_rcp_f32_e32 v223, v223
	v_pk_mul_f32 v[224:225], v[224:225], v[216:217]
	v_pk_mul_f32 v[226:227], v[226:227], v[218:219]
	v_pk_mul_f32 v[228:229], v[228:229], v[220:221]
	v_pk_mul_f32 v[230:231], v[230:231], v[222:223]
	v_med3_f32 v224, v224, s66, v202
	v_med3_f32 v225, v225, s66, v202
	v_med3_f32 v226, v226, s66, v202
	v_med3_f32 v227, v227, s66, v202
	v_med3_f32 v228, v228, s66, v202
	v_med3_f32 v229, v229, s66, v202
	v_med3_f32 v230, v230, s66, v202
	v_med3_f32 v231, v231, s66, v202
	v_cvt_pk_fp8_f32 v2, v224, v225
	v_cvt_pk_fp8_f32 v3, v228, v229
	v_cvt_pk_fp8_f32 v2, v226, v227 op_sel:[0,0,1]
	v_cvt_pk_fp8_f32 v3, v230, v231 op_sel:[0,0,1]
	s_nop 0
	global_store_dwordx2 v[0:1], v[2:3], off
	v_lshl_add_u64 v[0:1], v[0:1], 0, s[24:25]
	v_mul_f32_e32 v212, 0xbfb8aa3b, v211
	v_mul_f32_e32 v214, v211, v211
	v_pk_mul_f32 v[224:225], v[44:45], v[36:37]
	v_pk_mul_f32 v[226:227], v[46:47], v[38:39]
	v_pk_mul_f32 v[228:229], v[40:41], v[32:33]
	v_pk_mul_f32 v[230:231], v[42:43], v[34:35]
	v_mul_f32_e32 v214, 0x41000000, v214
	v_pk_mul_f32 v[216:217], v[44:45], v[212:213] op_sel_hi:[1,0]
	v_pk_mul_f32 v[218:219], v[46:47], v[212:213] op_sel_hi:[1,0]
	v_pk_mul_f32 v[220:221], v[40:41], v[212:213] op_sel_hi:[1,0]
	v_pk_mul_f32 v[222:223], v[42:43], v[212:213] op_sel_hi:[1,0]
	v_rcp_f32_e32 v214, v214
	v_exp_f32_e32 v216, v216
	v_exp_f32_e32 v217, v217
	v_exp_f32_e32 v218, v218
	v_exp_f32_e32 v219, v219
	v_exp_f32_e32 v220, v220
	v_exp_f32_e32 v221, v221
	v_exp_f32_e32 v222, v222
	v_exp_f32_e32 v223, v223
	v_pk_fma_f32 v[216:217], v[216:217], v[214:215], v[214:215] op_sel_hi:[1,0,0]
	v_pk_fma_f32 v[218:219], v[218:219], v[214:215], v[214:215] op_sel_hi:[1,0,0]
	v_pk_fma_f32 v[220:221], v[220:221], v[214:215], v[214:215] op_sel_hi:[1,0,0]
	v_pk_fma_f32 v[222:223], v[222:223], v[214:215], v[214:215] op_sel_hi:[1,0,0]
	v_rcp_f32_e32 v216, v216
	v_rcp_f32_e32 v217, v217
	v_rcp_f32_e32 v218, v218
	v_rcp_f32_e32 v219, v219
	v_rcp_f32_e32 v220, v220
	v_rcp_f32_e32 v221, v221
	v_rcp_f32_e32 v222, v222
	v_rcp_f32_e32 v223, v223
	v_pk_mul_f32 v[224:225], v[224:225], v[216:217]
	v_pk_mul_f32 v[226:227], v[226:227], v[218:219]
	v_pk_mul_f32 v[228:229], v[228:229], v[220:221]
	v_pk_mul_f32 v[230:231], v[230:231], v[222:223]
	v_med3_f32 v224, v224, s66, v202
	v_med3_f32 v225, v225, s66, v202
	v_med3_f32 v226, v226, s66, v202
	v_med3_f32 v227, v227, s66, v202
	v_med3_f32 v228, v228, s66, v202
	v_med3_f32 v229, v229, s66, v202
	v_med3_f32 v230, v230, s66, v202
	v_med3_f32 v231, v231, s66, v202
	v_cvt_pk_fp8_f32 v2, v224, v225
	v_cvt_pk_fp8_f32 v3, v228, v229
	v_cvt_pk_fp8_f32 v2, v226, v227 op_sel:[0,0,1]
	v_cvt_pk_fp8_f32 v3, v230, v231 op_sel:[0,0,1]
	s_nop 0
	global_store_dwordx2 v[0:1], v[2:3], off
	s_and_b64 vcc, exec, s[8:9]
	s_mov_b64 s[8:9], -1
	s_cbranch_vccnz .LBB0_2084
	s_and_b64 vcc, exec, s[4:5]
	s_cbranch_vccnz .LBB0_2083
	s_barrier
	s_branch .LBB0_2083
